# MoE GEMM phases: XCD-contiguous unit deal (c = (bid%8)*32 + bid/8) so the column tiles of a row tile and the row tiles of an expert share one XCD's L2
# speedup vs baseline: 1.0196x; 1.0099x over previous
; #define LAS __attribute__((address_space(3)))
; DI void moe_tables(const Params& p, LAS int* MT, int layer) {
;     const int tid = threadIdx.x;
;     __syncthreads();
;     if (tid < 64) {
;         const int e = tid & 31;
;         const int c = ((const int*)(p.ws + WS_CTL + CW_CNT))[layer * NEXP + e];
;         const int t = (c + 255) >> 8;
;         int incl = t;
; #pragma unroll
;         for (int off = 1; off < 32; off <<= 1) { const int y = __shfl_up(incl, off, 32); if (e >= off) incl += y; }
;         const int tp = incl - t;
;         if (tid < 32) {
;             MT[128 + e] = c; MT[e] = tp * 256; MT[64 + e] = tp;
;             for (int k = 0; k < t; ++k) MT[192 + tp + k] = e;
;             if (e == 31) { MT[32] = incl * 256; MT[64 + 32] = incl; }
;         }
;     }
;     __syncthreads();
; }
; __global__ void __launch_bounds__(NTHREADS, 2) fwd_kernel(Params p) {
;     ...
;     if (IN(8)) for (int rep_ = 0; rep_ <= REP(8); ++rep_) { if (rep_) __syncthreads();
;         moe_tables(p, MT, 0);
;     ...
;         MoeSchedUpT<true, 127 - 6> S; S.Hb = (const char*)(ws + WS_H8); S.EG = (const char*)(ws + WS_EG); S.LIST = (const int*)(ws + WS_LIST); S.MT = MT; S.K = DM / 2;
;         S.lda = DM; S.ldb = DM; S.a_h = 0; S.b_h = WS_EU - WS_EG; S.G = G; S.c = bid; S.estride = (size_t)EFF * DM; S.wscale = 127 - 6;
.LBB0_850:
	s_cmp_gt_i32 s24, 8
	s_cselect_b64 s[0:1], -1, 0
	s_cmp_lt_i32 s25, 9
	s_cselect_b64 s[2:3], -1, 0
	s_or_b64 s[0:1], s[0:1], s[2:3]
	s_and_b64 vcc, exec, s[0:1]
	s_cbranch_vccnz .LBB0_1009
	s_and_b32 s98, s22, 7
	s_lshl_b32 s98, s98, 5
	s_lshr_b32 s99, s22, 3
	s_or_b32 s98, s98, s99
	s_cmpk_lg_i32 s23, 0x100
	s_cselect_b32 s98, s22, s98
	s_waitcnt vmcnt(0)
	s_barrier
	s_and_saveexec_b64 s[0:1], s[20:21]
	s_cbranch_execz .LBB0_868
	v_and_b32_e32 v1, 31, v0
	v_lshlrev_b32_e32 v2, 2, v1
	v_mov_b32_e32 v3, 0
	v_lshl_add_u64 v[2:3], s[50:51], 0, v[2:3]
	v_add_co_u32_e32 v2, vcc, 0x4000, v2
	s_nop 1
	v_addc_co_u32_e32 v3, vcc, 0, v3, vcc
	global_load_dword v5, v[2:3], off
	v_mbcnt_lo_u32_b32 v2, -1, 0
	v_mbcnt_hi_u32_b32 v3, -1, v2
	v_and_b32_e32 v4, 0x60, v3
	v_add_u32_e32 v2, -1, v3
	v_cmp_lt_i32_e32 vcc, v2, v4
	v_add_u32_e32 v6, -2, v3
	v_add_u32_e32 v7, -4, v3
	v_cndmask_b32_e32 v2, v2, v3, vcc
	v_lshlrev_b32_e32 v9, 2, v2
	v_cmp_lt_i32_e32 vcc, v6, v4
	v_add_u32_e32 v8, -8, v3
	s_waitcnt vmcnt(0)
	v_add_u32_e32 v2, 0xff, v5
	v_ashrrev_i32_e32 v2, 8, v2
	ds_bpermute_b32 v9, v9, v2
	v_cndmask_b32_e32 v6, v6, v3, vcc
	v_cmp_ne_u32_e32 vcc, 0, v1
	v_lshlrev_b32_e32 v6, 2, v6
	s_waitcnt lgkmcnt(0)
	v_cndmask_b32_e32 v9, 0, v9, vcc
	v_add_u32_e32 v9, v9, v2
	ds_bpermute_b32 v6, v6, v9
	v_cmp_lt_i32_e32 vcc, v7, v4
	s_nop 1
	v_cndmask_b32_e32 v7, v7, v3, vcc
	v_cmp_lt_u32_e32 vcc, 1, v1
	v_lshlrev_b32_e32 v7, 2, v7
	s_waitcnt lgkmcnt(0)
	v_cndmask_b32_e32 v6, 0, v6, vcc
	v_add_u32_e32 v6, v6, v9
	ds_bpermute_b32 v7, v7, v6
	v_cmp_lt_i32_e32 vcc, v8, v4
	s_nop 1
	v_cndmask_b32_e32 v8, v8, v3, vcc
	v_cmp_lt_u32_e32 vcc, 3, v1
	v_lshlrev_b32_e32 v8, 2, v8
	s_waitcnt lgkmcnt(0)
	v_cndmask_b32_e32 v7, 0, v7, vcc
	v_add_u32_e32 v6, v7, v6
	ds_bpermute_b32 v7, v8, v6
	v_add_u32_e32 v8, -16, v3
	v_cmp_lt_i32_e32 vcc, v8, v4
	s_nop 1
	v_cndmask_b32_e32 v4, v8, v3, vcc
	v_cmp_lt_u32_e32 vcc, 7, v1
	v_lshlrev_b32_e32 v4, 2, v4
	s_waitcnt lgkmcnt(0)
	v_cndmask_b32_e32 v3, 0, v7, vcc
	v_add_u32_e32 v3, v3, v6
	ds_bpermute_b32 v4, v4, v3
	v_cmp_gt_u32_e32 vcc, 32, v0
	s_and_b64 exec, exec, vcc
	s_cbranch_execz .LBB0_868
	v_cmp_lt_u32_e32 vcc, 15, v1
	s_add_i32 s2, 0, 0x22040
	v_lshl_add_u32 v7, v1, 2, s2
	s_waitcnt lgkmcnt(0)
	v_cndmask_b32_e32 v4, 0, v4, vcc
	v_add_u32_e32 v3, v4, v3
	v_sub_u32_e32 v4, v3, v2
	v_lshlrev_b32_e32 v8, 8, v4
	v_cmp_lt_i32_e32 vcc, 0, v2
	v_lshl_add_u32 v6, v0, 2, s2
	ds_write_b32 v7, v8
	ds_write2st64_b32 v6, v4, v5 offset0:1 offset1:2
	s_and_saveexec_b64 s[2:3], vcc
	s_cbranch_execz .LBB0_866
	v_cmp_ne_u32_e32 vcc, 1, v2
	s_mov_b64 s[6:7], -1
	v_mov_b32_e32 v5, 0
	s_and_saveexec_b64 s[4:5], vcc
	s_cbranch_execz .LBB0_863
	v_add_u32_e32 v6, -2, v2
	v_lshrrev_b32_e32 v5, 1, v6
	v_add_u32_e32 v5, 1, v5
	v_cmp_lt_u32_e32 vcc, 13, v6
	v_mov_b32_e32 v8, 0
	s_and_saveexec_b64 s[6:7], vcc
	s_cbranch_execz .LBB0_859
	v_lshl_add_u32 v7, v4, 2, 0
	v_and_b32_e32 v6, -8, v5
	s_mov_b32 s10, 0
	v_add_u32_e32 v7, 0x22340, v7
	s_mov_b64 s[8:9], 0

;     DI bool next(int i, pg8::GU& u) const { int pm, pn; if (!T.tile(i, pm, pn)) return false; u.pm = pm; u.pn = pn; u.e = 0; u.aux = 0; u.h1 = 0; u.a = A + (size_t)pm * 256 * lda; u.b = Bt + (size_t)pn * 256 * ldb; return true; }
;     DI bool next(int i, pg8::GU& u) const {
;         const int L = i * G + c, T = MT[64 + 32]; if (L >= T * 4) return false;
;         const int rt = L >> 2, ct = L & 3; const int e = MT[192 + rt];
;         const int lt = rt - MT[64 + e];
;         u.e = e; u.pm = lt; u.pn = ct; u.aux = MT[e] + 256 * lt; u.h1 = (MT[128 + e] - 256 * lt) <= 128; u.a = Hb; u.b = EG + (size_t)e * estride + (size_t)ct * 128 * ldb; return true;
;     }
.LBB0_868:
	s_or_b64 exec, exec, s[0:1]
	s_add_u32 s0, s50, 0x41b76000
	s_addc_u32 s1, s51, 0
	s_add_u32 s27, s50, 0x310e000
	s_addc_u32 s68, s51, 0
	s_add_i32 s2, 0, 0x221c0
	v_mov_b32_e32 v1, s2
	s_waitcnt lgkmcnt(0)
	s_barrier
	ds_read_b32 v1, v1
	s_and_b32 s93, s98, 3
	v_lshrrev_b32_e32 v2, 3, v0
	v_readfirstlane_b32 s8, v0
	s_waitcnt lgkmcnt(0)
	v_readfirstlane_b32 s2, v1
	s_lshl_b32 s9, s2, 2
	s_cmp_lt_i32 s98, s9
	s_cselect_b64 s[6:7], -1, 0
	s_cmp_ge_i32 s98, s9
	s_mov_b32 s2, 0
	s_cbranch_scc1 .LBB0_870
	s_and_b32 s2, s98, -4
	s_add_i32 s3, 0, 0x22040
	s_add_i32 s2, s3, s2
	v_mov_b32_e32 v1, s2
	ds_read_b32 v3, v1 offset:768
	s_lshr_b32 s2, s98, 2
	s_lshl_b32 s4, s93, 18
	s_add_u32 s10, s27, s4
	s_mov_b64 s[40:41], s[0:1]
	s_waitcnt lgkmcnt(0)
	v_lshlrev_b32_e32 v1, 2, v3
	v_add_u32_e32 v1, s3, v1
	ds_read2st64_b32 v[4:5], v1 offset1:1
	ds_read_b32 v1, v1 offset:512
	s_addc_u32 s3, s68, 0
	v_readfirstlane_b32 s4, v3
	s_ashr_i32 s5, s4, 31
	s_waitcnt lgkmcnt(1)
	v_readfirstlane_b32 s11, v5
	s_sub_i32 s2, s2, s11
	s_lshl_b32 s2, s2, 8
	s_waitcnt lgkmcnt(0)
	v_subrev_u32_e32 v1, s2, v1
	s_movk_i32 s11, 0x81
	s_lshl_b64 s[4:5], s[4:5], 20
	v_cmp_gt_i32_e32 vcc, s11, v1
	s_add_u32 s4, s10, s4
	v_add_u32_e32 v239, s2, v4
	v_cndmask_b32_e64 v10, 0, 1, vcc
	s_addc_u32 s5, s3, s5
	s_branch .LBB0_871

;     DI bool next(int i, pg8::GU& u) const { int pm, pn; if (!T.tile(i, pm, pn)) return false; u.pm = pm; u.pn = pn; u.e = 0; u.aux = 0; u.h1 = 0; u.a = A + (size_t)pm * 256 * lda; u.b = Bt + (size_t)pn * 256 * ldb; return true; }
;     DI bool next(int i, pg8::GU& u) const {
;         const int L = i * G + c, T = MT[64 + 32]; if (L >= T * 4) return false;
;         const int rt = L >> 2, ct = L & 3; const int e = MT[192 + rt];
;         const int lt = rt - MT[64 + e];
;         u.e = e; u.pm = lt; u.pn = ct; u.aux = MT[e] + 256 * lt; u.h1 = (MT[128 + e] - 256 * lt) <= 128; u.a = Hb; u.b = EG + (size_t)e * estride + (size_t)ct * 128 * ldb; return true;
.LBB0_885:
	ds_read_b32 v2, v226
	s_add_i32 s77, s77, 1
	s_mul_i32 s2, s77, s23
	s_add_i32 s2, s2, s98
	s_waitcnt lgkmcnt(0)
	v_readfirstlane_b32 s3, v2
	s_lshl_b32 s3, s3, 2
	s_cmp_lt_i32 s2, s3
	s_cselect_b64 s[6:7], -1, 0
	s_cmp_ge_i32 s2, s3
	s_cbranch_scc1 .LBB0_887
	s_and_b32 s3, s2, -4
	s_add_i32 s3, s85, s3
	v_mov_b32_e32 v2, s3
	ds_read_b32 v232, v2 offset:768
	s_ashr_i32 s8, s2, 2
	s_and_b32 s91, s2, 3
	s_mov_b64 s[34:35], s[0:1]
	s_waitcnt lgkmcnt(0)
	v_lshlrev_b32_e32 v2, 2, v232
	v_add_u32_e32 v4, s85, v2
	ds_read2st64_b32 v[2:3], v4 offset1:1
	ds_read_b32 v4, v4 offset:512
	v_readfirstlane_b32 s2, v232
	s_ashr_i32 s3, s2, 31
	s_lshl_b64 s[2:3], s[2:3], 20
	s_waitcnt lgkmcnt(0)
	v_readfirstlane_b32 s9, v3
	s_sub_i32 s92, s8, s9
	s_lshl_b32 s8, s92, 8
	s_add_u32 s2, s27, s2
	v_add_u32_e32 v233, s8, v2
	v_subrev_u32_e32 v2, s8, v4
	s_addc_u32 s3, s68, s3
	s_lshl_b32 s8, s91, 18
	v_cmp_gt_i32_e32 vcc, s86, v2
	s_add_u32 s30, s2, s8
	s_addc_u32 s31, s3, 0
	v_cndmask_b32_e64 v234, 0, 1, vcc

; DI void cvt_group(const Params& p, LAS unsigned char* lds, int group, int t_lo, int t_hi, int r, int I) {
;     ...
;     if (tid == 0) {
;         int t0 = 0, nj = 0;
;         if (group == 0) {
;             set_job(J, 0, p.in[11], (bf16_t*)(ws + WS_W0IN), DM, L0IN, DM, 0, 1, 0, 0, t0);
;             set_job(J, 1, p.in[13], (bf16_t*)(ws + WS_WUQ), 512, 1536, 512, 0, 1, 0, 0, t0);
;             set_job(J, 2, p.in[15], (bf16_t*)(ws + WS_WUKV), 256, 2048, 256, 0, 1, 0, 0, t0);
;             set_job(J, 3, p.in[23], (bf16_t*)(ws + WS_W0OUT), DM, DM, DM, 0, 1, 0, 0, t0);
;             set_job(J, 4, p.in[31], (bf16_t*)(ws + WS_W1IN), DM, L1IN, DM, 1, 1, 0, 0, t0); if (FP8_IN1) J[4].f8scale = 64.f;
;             set_job(J, 5, p.in[34], (bf16_t*)(ws + WS_W1OUT), DM, DM, DM, 0, 1, 0, 0, t0); if (FP8_OUT1) J[5].f8scale = 64.f;
;             set_job(J, 6, p.in[18], (bf16_t*)(ws + WS_GW), 128, 128, 128, 0, 16, 128 * 128, 128 * 128, t0);
;             set_job(J, 7, p.in[20], (bf16_t*)(ws + WS_GW + (size_t)16 * 128 * 128 * 2), 128, 128, 128, 0, 16, 128 * 128, 128 * 128, t0);
;             nj = 8;
;         } else if (group == 1) {
;             set_job(J, 0, p.in[24], (bf16_t*)(ws + WS_EG), DM, EFF, DM, 0, NEXP, (size_t)DM * EFF, (size_t)EFF * DM, t0);
;             set_job(J, 1, p.in[25], (bf16_t*)(ws + WS_EU), DM, EFF, DM, 0, NEXP, (size_t)DM * EFF, (size_t)EFF * DM, t0);
;             set_job(J, 2, p.in[26], (bf16_t*)(ws + WS_ED), EFF, DM, EFF, 0, NEXP, (size_t)DM * EFF, (size_t)EFF * DM, t0);
;             if (FP8_L0) { J[0].f8scale = 64.f; J[1].f8scale = 64.f; J[2].f8scale = 32.f; }
;             nj = 3;
;         } else {
;             set_job(J, 0, p.in[35], (bf16_t*)(ws + WS_EG + EXPW), DM, EFF, DM, 0, NEXP, (size_t)DM * EFF, (size_t)EFF * DM, t0); J[0].f8scale = 64.f;
;             set_job(J, 1, p.in[36], (bf16_t*)(ws + WS_EU + EXPW), DM, EFF, DM, 0, NEXP, (size_t)DM * EFF, (size_t)EFF * DM, t0); J[1].f8scale = 64.f;
;             set_job(J, 2, p.in[37], (bf16_t*)(ws + WS_ED + EXPW), EFF, DM, EFF, 0, NEXP, (size_t)DM * EFF, (size_t)EFF * DM, t0); J[2].f8scale = 32.f;
;             nj = 3;
;         }
;         J[nj].tile0 = t0; J[15].tile0 = nj;
;     }
;     __syncthreads();
;     const int nj = J[15].tile0, total = J[nj].tile0;
;     const int hi = min(t_hi, total);
;     const int row = tid >> 6, c4 = (tid & 63) * 4;
;     for (int gt = t_lo + r; gt < hi; gt += I) {
.LBB0_915:
	s_add_u32 s18, s50, 0x710e000
	s_addc_u32 s19, s51, 0
	s_add_u32 s16, s50, 0xf10e000
	s_addc_u32 s17, s51, 0
	s_add_u32 s14, s50, 0x1710e000
	s_addc_u32 s15, s51, 0
	s_abs_i32 s0, s23
	v_cvt_f32_u32_e32 v3, s0
	s_sub_i32 s5, 0, s0
	s_abs_i32 s4, s9
	s_ashr_i32 s1, s9, 31
	v_rcp_iflag_f32_e32 v3, v3
	v_and_b32_e32 v11, 0xff, v0
	v_lshlrev_b32_e32 v4, 1, v0
	v_mul_u32_u24_e32 v2, 0x410, v198
	v_mul_f32_e32 v3, 0x4f7ffffe, v3
	v_cvt_u32_f32_e32 v3, v3
	v_and_b32_e32 v10, 0xfc, v199
	v_and_b32_e32 v4, 32, v4
	v_lshl_add_u32 v16, v11, 2, 0
	v_readfirstlane_b32 s6, v3
	s_mul_i32 s5, s5, s6
	s_mul_hi_u32 s5, s6, s5
	s_add_i32 s6, s6, s5
	s_mul_hi_u32 s5, s4, s6
	s_mul_i32 s5, s5, s0
	s_sub_i32 s4, s4, s5
	s_sub_i32 s5, s4, s0
	s_cmp_ge_u32 s4, s0
	s_cselect_b32 s4, s5, s4
	s_sub_i32 s5, s4, s0
	s_cmp_ge_u32 s4, s0
	s_cselect_b32 s0, s5, s4
	s_xor_b32 s0, s0, s1
	s_sub_i32 s4, s0, s1
	v_mul_u32_u24_e32 v14, 0x410, v222
	v_mul_u32_u24_e32 v13, 0x410, v223
	v_cmp_eq_u32_e64 s[2:3], 0, v0
	v_mov_b32_e32 v199, 0
	v_lshl_add_u32 v15, v10, 2, 0
	v_and_or_b32 v1, v1, 16, v4
	s_cmp_lg_u32 s4, 0
	v_add_u32_e32 v12, v16, v2
	s_cbranch_scc0 .LBB0_938
	s_cmp_lt_i32 s98, s4
	s_cbranch_scc1 .LBB0_937
	s_waitcnt vmcnt(0)
	s_barrier
	s_and_saveexec_b64 s[0:1], s[2:3]
	s_cbranch_execz .LBB0_919
	s_movk_i32 s8, 0x800
	s_mov_b32 s11, 0
	s_add_i32 s5, 0, 0x12000
	s_mov_b32 s10, s8
	v_mov_b32_e32 v2, s42
	v_mov_b32_e32 v3, s43
	v_mov_b32_e32 v4, s18
	v_mov_b32_e32 v5, s19
	v_mov_b32_e32 v6, s5
	s_movk_i32 s9, 0x200
	s_add_i32 s5, 0, 0x12010
	v_mov_b64_e32 v[24:25], s[10:11]
	ds_write_b128 v6, v[2:5]
	v_mov_b32_e32 v2, s5
	v_mov_b64_e32 v[22:23], s[8:9]
	s_add_i32 s5, 0, 0x12020
	s_mov_b32 s6, 0x100000
	ds_write_b128 v2, v[22:25]
	v_mov_b32_e32 v8, 64
	v_mov_b32_e32 v9, 0
	v_mov_b32_e32 v2, s5
	s_add_i32 s5, 0, 0x12028
	s_mov_b32 s7, s11
	s_mov_b32 s10, s6
	ds_write_b64 v2, v[8:9]
	v_mov_b32_e32 v2, s5
	v_mov_b64_e32 v[18:19], s[6:7]
	v_mov_b64_e32 v[20:21], s[10:11]
	s_add_i32 s5, 0, 0x12040
	ds_write2_b64 v2, v[18:19], v[20:21] offset1:1
	v_mov_b32_e32 v2, s44
	v_mov_b32_e32 v3, s45
	v_mov_b32_e32 v4, s16
	v_mov_b32_e32 v5, s17
	v_mov_b32_e32 v6, s5
	s_add_i32 s5, 0, 0x12050
	ds_write_b128 v6, v[2:5]
	v_mov_b32_e32 v2, s5
	s_add_i32 s5, 0, 0x12060
	ds_write_b128 v2, v[22:25]
	v_mov_b32_e32 v3, 0x800
	v_mov_b32_e32 v2, v8
	v_mov_b32_e32 v4, s5
	s_add_i32 s5, 0, 0x12068
	ds_write_b64 v4, v[2:3]
	v_mov_b32_e32 v2, s5
	s_add_i32 s5, 0, 0x12080
	ds_write2_b64 v2, v[18:19], v[20:21] offset1:1
	v_mov_b32_e32 v4, s46
	v_mov_b32_e32 v5, s47
	v_mov_b32_e32 v6, s14
	v_mov_b32_e32 v7, s15
	v_mov_b32_e32 v2, s5
	ds_write_b128 v2, v[4:7]
	v_mov_b32_e32 v2, 0x200
	s_add_i32 s5, 0, 0x12090
	v_mov_b32_e32 v4, v2
	v_mov_b32_e32 v5, v9
	v_mov_b32_e32 v6, s5
	s_add_i32 s5, 0, 0x120a0
	ds_write_b128 v6, v[2:5]
	v_mov_b32_e32 v9, 0x1000
	v_mov_b32_e32 v2, s5
	s_add_i32 s5, 0, 0x120a8
	ds_write_b64 v2, v[8:9]
	v_mov_b32_e32 v2, s5
	s_add_i32 s5, 0, 0x12038
	ds_write2_b64 v2, v[18:19], v[20:21] offset1:1
	v_mov_b32_e32 v2, 0x42800000
	v_mov_b32_e32 v3, s5
	s_add_i32 s5, 0, 0x12078
	ds_write_b32 v3, v2
	v_mov_b32_e32 v3, s5
	s_add_i32 s5, 0, 0x120b8
	ds_write_b32 v3, v2
	v_mov_b32_e32 v2, 0x42000000
	v_mov_b32_e32 v3, s5
	s_add_i32 s5, 0, 0x120e4
	ds_write_b32 v3, v2
	v_mov_b32_e32 v2, 0x1800
	v_mov_b32_e32 v3, s5
	s_add_i32 s5, 0, 0x123e4
	ds_write_b32 v3, v2
	v_mov_b32_e32 v2, 3
	v_mov_b32_e32 v3, s5
	ds_write_b32 v3, v2
.LBB0_919:
	s_or_b64 exec, exec, s[0:1]
	s_add_i32 s0, 0, 0x123e4
	v_mov_b32_e32 v2, s0
	s_waitcnt lgkmcnt(0)
	s_barrier
	ds_read_b32 v2, v2
	s_sub_i32 s27, s98, s4
	s_waitcnt lgkmcnt(0)
	v_lshlrev_b32_e32 v3, 6, v2
	v_add_u32_e32 v3, 0, v3
	v_add_u32_e32 v3, 0x12024, v3
	ds_read_b32 v3, v3
	v_readfirstlane_b32 s30, v2
	s_waitcnt lgkmcnt(0)
	v_min_i32_e32 v17, 0x960, v3
	v_cmp_ge_i32_e32 vcc, s27, v17
	s_cbranch_vccnz .LBB0_937
	s_sub_i32 s31, s23, s4
	s_cmp_gt_i32 s30, 1
	s_cselect_b64 s[0:1], -1, 0
	s_add_i32 s4, s30, -1
	s_cmp_lg_u32 s30, 2
	v_cndmask_b32_e64 v2, 0, 1, s[0:1]
	s_cselect_b64 s[0:1], -1, 0
	s_and_b32 s34, s4, -2
	s_or_b32 s35, s4, 1
	s_cmp_lg_u32 s4, s34
	v_cndmask_b32_e64 v4, 0, 1, s[0:1]
	s_cselect_b64 s[8:9], -1, 0
	v_cmp_ne_u32_e64 s[4:5], 1, v2
	s_add_i32 s40, 0, 0x120a4
	s_brev_b32 s41, 1
	v_lshlrev_b32_e32 v2, 2, v10
	v_mov_b32_e32 v3, 0
	v_add_u32_e32 v18, v15, v14
	s_movk_i32 s54, 0x4ff
	s_movk_i32 s55, 0xffcf
	s_mov_b32 s58, 0xc3e00000
	v_cmp_ne_u32_e64 s[6:7], 1, v4
	v_mov_b32_e32 v19, 0x43e00000
	s_branch .LBB0_923

; #define LAS __attribute__((address_space(3)))
; DI void cvt_group(const Params& p, LAS unsigned char* lds, int group, int t_lo, int t_hi, int r, int I) {
;     ...
;     __syncthreads();
;     const int nj = J[15].tile0, total = J[nj].tile0;
;     const int hi = min(t_hi, total);
;     const int row = tid >> 6, c4 = (tid & 63) * 4;
;     for (int gt = t_lo + r; gt < hi; gt += I) {
;         CvtTile cur; cvt_decode(J, nj, gt, cur);
; DI void bg_range(const Params& p, LAS unsigned char* lds, int group, int t_lo, int t_hi, int nunits, int G, int bid) {
;     const int rem = nunits % G;
;     if (rem == 0) cvt_group(p, lds, group, t_lo, t_hi, bid, G);
;     else if (bid >= rem) cvt_group(p, lds, group, t_lo, t_hi, bid - rem, G - rem);
.LBB0_941:
	s_or_b64 exec, exec, s[0:1]
	s_add_i32 s0, 0, 0x123e4
	v_mov_b32_e32 v2, s0
	s_waitcnt lgkmcnt(0)
	s_barrier
	ds_read_b32 v2, v2
	s_waitcnt lgkmcnt(0)
	v_lshlrev_b32_e32 v3, 6, v2
	v_add_u32_e32 v3, 0, v3
	v_add_u32_e32 v3, 0x12024, v3
	ds_read_b32 v3, v3
	v_readfirstlane_b32 s15, v2
	s_waitcnt lgkmcnt(0)
	v_readfirstlane_b32 s0, v3
	s_min_i32 s14, s0, 0x960
	s_cmp_ge_i32 s98, s14
	s_cbranch_scc1 .LBB0_959
	s_cmp_gt_i32 s15, 1
	s_cselect_b64 s[0:1], -1, 0
	s_add_i32 s4, s15, -1
	s_cmp_lg_u32 s15, 2
	v_cndmask_b32_e64 v2, 0, 1, s[0:1]
	s_cselect_b64 s[0:1], -1, 0
	s_and_b32 s16, s4, -2
	s_or_b32 s17, s4, 1
	s_cmp_lg_u32 s4, s16
	v_cndmask_b32_e64 v4, 0, 1, s[0:1]
	s_cselect_b64 s[8:9], -1, 0
	v_cmp_ne_u32_e64 s[4:5], 1, v2
	s_add_i32 s18, 0, 0x120a4
	s_brev_b32 s19, 1
	v_lshlrev_b32_e32 v2, 2, v10
	v_mov_b32_e32 v3, 0
	v_add_u32_e32 v14, v15, v14
	s_movk_i32 s27, 0x4ff
	s_movk_i32 s30, 0xffcf
	s_mov_b32 s31, 0xc3e00000
	v_cmp_ne_u32_e64 s[6:7], 1, v4
	v_add_u32_e32 v13, v16, v13
	v_mov_b32_e32 v15, 0x43e00000
	s_mov_b32 s34, s98
	s_branch .LBB0_945

; #define LAS __attribute__((address_space(3)))
; DI void moe_tables(const Params& p, LAS int* MT, int layer) {
;     const int tid = threadIdx.x;
;     __syncthreads();
;     if (tid < 64) {
;         const int e = tid & 31;
;         const int c = ((const int*)(p.ws + WS_CTL + CW_CNT))[layer * NEXP + e];
;         const int t = (c + 255) >> 8;
;         int incl = t;
; #pragma unroll
;         for (int off = 1; off < 32; off <<= 1) { const int y = __shfl_up(incl, off, 32); if (e >= off) incl += y; }
;         const int tp = incl - t;
;         if (tid < 32) {
;             MT[128 + e] = c; MT[e] = tp * 256; MT[64 + e] = tp;
;             for (int k = 0; k < t; ++k) MT[192 + tp + k] = e;
;             if (e == 31) { MT[32] = incl * 256; MT[64 + 32] = incl; }
;         }
;     }
;     __syncthreads();
; }
; __global__ void __launch_bounds__(NTHREADS, 2) fwd_kernel(Params p) {
;     ...
;     if (IN(9)) for (int rep_ = 0; rep_ <= REP(9); ++rep_) { if (rep_) __syncthreads();
;         moe_tables(p, MT, 0);
;     ...
;         MoeSchedDownT<true, 127 - 5> S; S.ACT = (const char*)(ws + WS_ACT); S.ED = (const char*)(ws + WS_ED); S.MT = MT; S.K = EFF / 2;
;         S.lda = EFF; S.ldb = EFF; S.a_h = 128 * EFF; S.b_h = 128 * EFF; S.G = G; S.c = bid; S.estride = (size_t)DM * EFF; S.wscale = 127 - 5;
.LBB0_1009:
	s_cmp_gt_i32 s24, 9
	s_cselect_b64 s[0:1], -1, 0
	s_cmp_lt_i32 s25, 10
	s_cselect_b64 s[2:3], -1, 0
	s_or_b64 s[0:1], s[0:1], s[2:3]
	s_and_b64 vcc, exec, s[0:1]
	s_cbranch_vccnz .LBB0_1103
	s_and_b32 s98, s22, 7
	s_lshl_b32 s98, s98, 5
	s_lshr_b32 s99, s22, 3
	s_or_b32 s98, s98, s99
	s_cmpk_lg_i32 s23, 0x100
	s_cselect_b32 s98, s22, s98
	s_waitcnt vmcnt(0)
	s_barrier
	s_and_saveexec_b64 s[0:1], s[20:21]
	s_cbranch_execz .LBB0_1027
	v_and_b32_e32 v1, 31, v0
	v_lshlrev_b32_e32 v2, 2, v1
	v_mov_b32_e32 v3, 0
	v_lshl_add_u64 v[2:3], s[50:51], 0, v[2:3]
	v_add_co_u32_e32 v2, vcc, 0x4000, v2
	s_nop 1
	v_addc_co_u32_e32 v3, vcc, 0, v3, vcc
	global_load_dword v5, v[2:3], off
	v_mbcnt_lo_u32_b32 v2, -1, 0
	v_mbcnt_hi_u32_b32 v3, -1, v2
	v_and_b32_e32 v4, 0x60, v3
	v_add_u32_e32 v2, -1, v3
	v_cmp_lt_i32_e32 vcc, v2, v4
	v_add_u32_e32 v6, -2, v3
	v_add_u32_e32 v7, -4, v3
	v_cndmask_b32_e32 v2, v2, v3, vcc
	v_lshlrev_b32_e32 v9, 2, v2
	v_cmp_lt_i32_e32 vcc, v6, v4
	v_add_u32_e32 v8, -8, v3
	s_waitcnt vmcnt(0)
	v_add_u32_e32 v2, 0xff, v5
	v_ashrrev_i32_e32 v2, 8, v2
	ds_bpermute_b32 v9, v9, v2
	v_cndmask_b32_e32 v6, v6, v3, vcc
	v_cmp_ne_u32_e32 vcc, 0, v1
	v_lshlrev_b32_e32 v6, 2, v6
	s_waitcnt lgkmcnt(0)
	v_cndmask_b32_e32 v9, 0, v9, vcc
	v_add_u32_e32 v9, v9, v2
	ds_bpermute_b32 v6, v6, v9
	v_cmp_lt_i32_e32 vcc, v7, v4
	s_nop 1
	v_cndmask_b32_e32 v7, v7, v3, vcc
	v_cmp_lt_u32_e32 vcc, 1, v1
	v_lshlrev_b32_e32 v7, 2, v7
	s_waitcnt lgkmcnt(0)
	v_cndmask_b32_e32 v6, 0, v6, vcc
	v_add_u32_e32 v6, v6, v9
	ds_bpermute_b32 v7, v7, v6
	v_cmp_lt_i32_e32 vcc, v8, v4
	s_nop 1
	v_cndmask_b32_e32 v8, v8, v3, vcc
	v_cmp_lt_u32_e32 vcc, 3, v1
	v_lshlrev_b32_e32 v8, 2, v8
	s_waitcnt lgkmcnt(0)
	v_cndmask_b32_e32 v7, 0, v7, vcc
	v_add_u32_e32 v6, v7, v6
	ds_bpermute_b32 v7, v8, v6
	v_add_u32_e32 v8, -16, v3
	v_cmp_lt_i32_e32 vcc, v8, v4
	s_nop 1
	v_cndmask_b32_e32 v4, v8, v3, vcc
	v_cmp_lt_u32_e32 vcc, 7, v1
	v_lshlrev_b32_e32 v4, 2, v4
	s_waitcnt lgkmcnt(0)
	v_cndmask_b32_e32 v3, 0, v7, vcc
	v_add_u32_e32 v3, v3, v6
	ds_bpermute_b32 v4, v4, v3
	v_cmp_gt_u32_e32 vcc, 32, v0
	s_and_b64 exec, exec, vcc
	s_cbranch_execz .LBB0_1027
	v_cmp_lt_u32_e32 vcc, 15, v1
	s_add_i32 s2, 0, 0x22040
	v_lshl_add_u32 v7, v1, 2, s2
	s_waitcnt lgkmcnt(0)
	v_cndmask_b32_e32 v4, 0, v4, vcc
	v_add_u32_e32 v3, v4, v3
	v_sub_u32_e32 v4, v3, v2
	v_lshlrev_b32_e32 v8, 8, v4
	v_cmp_lt_i32_e32 vcc, 0, v2
	v_lshl_add_u32 v6, v0, 2, s2
	ds_write_b32 v7, v8
	ds_write2st64_b32 v6, v4, v5 offset0:1 offset1:2
	s_and_saveexec_b64 s[2:3], vcc
	s_cbranch_execz .LBB0_1025
	v_cmp_ne_u32_e32 vcc, 1, v2
	s_mov_b64 s[6:7], -1
	v_mov_b32_e32 v5, 0
	s_and_saveexec_b64 s[4:5], vcc
	s_cbranch_execz .LBB0_1022
	v_add_u32_e32 v6, -2, v2
	v_lshrrev_b32_e32 v5, 1, v6
	v_add_u32_e32 v5, 1, v5
	v_cmp_lt_u32_e32 vcc, 13, v6
	v_mov_b32_e32 v8, 0
	s_and_saveexec_b64 s[6:7], vcc
	s_cbranch_execz .LBB0_1018
	v_lshl_add_u32 v7, v4, 2, 0
	v_and_b32_e32 v6, -8, v5
	s_mov_b32 s10, 0
	v_add_u32_e32 v7, 0x22340, v7
	s_mov_b64 s[8:9], 0

; #define PG8_STAGE_A(bufoff, gbase, h, VG) do { if constexpr (Sched::GATHER) { PG8_STAGE(bufoff, gbase, VG[h]); } else { PG8_STAGE(bufoff, (gbase) + (h) * ahs, voffA); } } while (0)
; #define PG8_STAGE_B(bufoff, gbase, h) PG8_STAGE(bufoff, (gbase) + (h) * bhs, voffB)
; #define PG8_WAIT_V(n) asm volatile("s_waitcnt vmcnt(" #n ")" ::: "memory")
; #define PG8_BAR __builtin_amdgcn_s_barrier()
;     DI unsigned rowoff(const pg8::GU& u, int r) const { const int gr = 256 * u.pm + r; const int tok = gr < MT[128 + u.e] ? LIST[(size_t)u.e * MOE_CAP + gr] : NTOK; return (unsigned)tok * (unsigned)lda; }
;     DI bool next(int i, pg8::GU& u) const { int pm, pn; if (!T.tile(i, pm, pn)) return false; u.pm = pm; u.pn = pn; u.e = 0; u.aux = 0; u.h1 = 0; u.a = A + (size_t)pm * 256 * lda; u.b = Bt + (size_t)pn * 256 * ldb; return true; }
; template <class Epi, class Sched>
; DI void gemm_phase(LAS unsigned char* lds, const Sched& S, const Epi& E) {
;     ...
;     if constexpr (Sched::GATHER) {
; #pragma unroll
;         for (int h = 0; h < 2; ++h)
; #pragma unroll
;             for (int i = 0; i < 2; ++i) { vc[h][i] = S.rowoff(cur, RR[i] + 128 * h) + (unsigned)(CC[i] * 2); vn[h][i] = vc[h][i]; }
;     } else {
; #pragma unroll
;         for (int h = 0; h < 2; ++h)
; #pragma unroll
;             for (int i = 0; i < 2; ++i) { vc[h][i] = 0u; vn[h][i] = 0u; }
;     }
;     const char* cA = cur.a; const char* cB = cur.b;
;     if constexpr (PG8_SP2) {
;         PG8_STAGE_B(PG8_SB(0, 0), cB, 0); PG8_STAGE_B(PG8_SB(0, 1), cB, 1); PG8_STAGE_A(PG8_SA(0, 0), cA, 0, vc); PG8_STAGE_A(PG8_SA(0, 1), cA, 1, vc);
;         if (wr == 1) PG8_BAR;
;         PG8_WAIT_V(2); PG8_BAR;
;         PG8_STAGE_B(PG8_SB(1, 0), cB + kstep, 0); PG8_STAGE_A(PG8_SA(1, 0), cA + kstep, 0, vc); PG8_STAGE_B(PG8_SB(1, 1), cB + kstep, 1);
;         PG8_WAIT_V(6); PG8_BAR;
;     DI bool next(int i, pg8::GU& u) const {
;         const int L = i * G + c, T = MT[64 + 32]; if (L >= T * 8) return false;
;         const int rt = L >> 3, ct = L & 7; const int e = MT[192 + rt];
;         const int lt = rt - MT[64 + e];
;         u.e = e; u.pm = lt; u.pn = ct; u.aux = MT[e] + 256 * lt; u.h1 = (MT[128 + e] - 256 * lt) <= 128; u.a = ACT + (size_t)u.aux * lda; u.b = ED + (size_t)e * estride + (size_t)ct * 256 * ldb; return true;
.LBB0_1027:
	s_or_b64 exec, exec, s[0:1]
	s_add_i32 s0, 0, 0x221c0
	v_mov_b32_e32 v1, s0
	s_waitcnt lgkmcnt(0)
	s_barrier
	ds_read_b32 v1, v1
	v_readfirstlane_b32 s2, v0
	s_waitcnt lgkmcnt(0)
	v_lshlrev_b32_e32 v1, 3, v1
	v_cmp_ge_i32_e32 vcc, s98, v1
	s_cbranch_vccnz .LBB0_1053
	v_lshrrev_b32_e32 v1, 5, v0
	v_lshrrev_b32_e32 v3, 1, v0
	s_lshr_b32 s4, s2, 6
	v_and_b32_e32 v1, 4, v1
	v_bfe_u32 v2, v0, 2, 2
	v_and_b32_e32 v10, 24, v3
	s_lshr_b32 s3, s2, 8
	s_lshl_b32 s8, s4, 10
	v_or3_b32 v1, v1, v2, v10
	v_lshlrev_b32_e32 v2, 4, v0
	v_bfe_u32 v3, v0, 3, 25
	v_and_b32_e32 v5, 32, v0
	s_add_u32 s27, s50, 0x32d76000
	v_or_b32_e32 v3, 64, v3
	s_movk_i32 s0, 0x60
	v_bitop3_b32 v2, v2, v5, 48 bitop3:0x6c
	s_addc_u32 s74, s51, 0
	v_and_or_b32 v4, v3, s0, v1
	v_and_or_b32 v2, v0, 64, v2
	s_add_u32 s75, s50, 0x1310e000
	v_lshl_or_b32 v198, v4, 9, v2
	v_bfe_u32 v4, v0, 2, 4
	s_movk_i32 s0, 0x70
	s_addc_u32 s76, s51, 0
	v_and_or_b32 v3, v3, s0, v4
	s_ashr_i32 s5, s98, 3
	v_lshl_or_b32 v200, v3, 9, v2
	v_lshrrev_b32_e32 v3, 3, v0
	s_add_i32 s77, 0, 0x22040
	s_lshl_b32 s0, s5, 2
	v_and_or_b32 v1, v3, 32, v1
	s_add_i32 s0, s77, s0
	v_lshl_or_b32 v202, v1, 9, v2
	v_and_or_b32 v1, v3, 48, v4
	v_mov_b32_e32 v3, s0
	ds_read_b32 v4, v3 offset:768
	v_lshl_or_b32 v204, v1, 9, v2
	s_and_b32 s97, s98, 7
	s_lshl_b32 s0, s97, 17
	s_add_u32 s9, s75, s0
	s_waitcnt lgkmcnt(0)
	v_lshlrev_b32_e32 v1, 2, v4
	v_add_u32_e32 v1, s77, v1
	ds_read2st64_b32 v[2:3], v1 offset1:1
	s_addc_u32 s10, s76, 0
	v_readfirstlane_b32 s0, v4
	s_ashr_i32 s1, s0, 31
	ds_read_b32 v1, v1 offset:512
	s_waitcnt lgkmcnt(1)
	v_readfirstlane_b32 s6, v3
	s_sub_i32 s5, s5, s6
	s_lshl_b32 s5, s5, 8
	v_readfirstlane_b32 s6, v2
	s_add_i32 s34, s5, s6
	s_ashr_i32 s35, s34, 31
	s_lshl_b64 s[6:7], s[34:35], 9
	s_add_u32 s54, s27, s6
	s_addc_u32 s55, s74, s7
	s_lshl_b64 s[0:1], s[0:1], 20
	s_add_u32 s58, s9, s0
	s_addc_u32 s59, s10, s1
	s_add_i32 s35, s8, 0
	s_add_i32 s78, s35, 0x10000
	s_add_i32 s79, s35, 0x12000
	s_mov_b32 m0, s78
	s_add_u32 s0, s58, 0x10000
	global_load_lds_dwordx4 v202, s[58:59]
	s_mov_b32 m0, s79
	s_addc_u32 s1, s59, 0
	s_add_i32 s80, s35, 0x14000
	global_load_lds_dwordx4 v198, s[58:59]
	s_mov_b32 m0, s80
	s_add_i32 s81, s35, 0x16000
	global_load_lds_dwordx4 v202, s[0:1]
	s_mov_b32 m0, s81
	s_add_i32 s82, s35, 0x2000
	global_load_lds_dwordx4 v198, s[0:1]
	s_mov_b32 m0, s35
	s_add_u32 s0, s54, 0x10000
	global_load_lds_dwordx4 v204, s[54:55]
	s_mov_b32 m0, s82
	s_addc_u32 s1, s55, 0
	s_add_i32 s83, s35, 0x4000
	global_load_lds_dwordx4 v200, s[54:55]
	s_mov_b32 m0, s83
	s_add_i32 s84, s35, 0x6000
	global_load_lds_dwordx4 v204, s[0:1]
	s_mov_b32 m0, s84
	v_mov_b32_e32 v66, 0
	global_load_lds_dwordx4 v200, s[0:1]
	v_mov_b32_e32 v203, v66
	v_mov_b32_e32 v199, v66
	v_mov_b32_e32 v205, v66
	v_mov_b32_e32 v201, v66
	s_cmp_eq_u32 s3, 1
	v_lshl_add_u64 v[8:9], s[58:59], 0, v[202:203]
	v_lshl_add_u64 v[6:7], s[58:59], 0, v[198:199]
	v_lshl_add_u64 v[2:3], s[54:55], 0, v[204:205]
	s_cselect_b64 s[0:1], -1, 0
	s_cmp_lg_u32 s3, 1
	v_lshl_add_u64 v[4:5], s[54:55], 0, v[200:201]
	s_cbranch_scc1 .LBB0_1030
	s_barrier

;     DI bool next(int i, pg8::GU& u) const { int pm, pn; if (!T.tile(i, pm, pn)) return false; u.pm = pm; u.pn = pn; u.e = 0; u.aux = 0; u.h1 = 0; u.a = A + (size_t)pm * 256 * lda; u.b = Bt + (size_t)pn * 256 * ldb; return true; }
;     DI bool next(int i, pg8::GU& u) const {
;         const int L = i * G + c, T = MT[64 + 32]; if (L >= T * 8) return false;
;         const int rt = L >> 3, ct = L & 7; const int e = MT[192 + rt];
;         const int lt = rt - MT[64 + e];
;         u.e = e; u.pm = lt; u.pn = ct; u.aux = MT[e] + 256 * lt; u.h1 = (MT[128 + e] - 256 * lt) <= 128; u.a = ACT + (size_t)u.aux * lda; u.b = ED + (size_t)e * estride + (size_t)ct * 256 * ldb; return true;
.LBB0_1033:
	ds_read_b32 v3, v213
	s_add_i32 s92, s92, 1
	s_mul_i32 s2, s92, s23
	s_add_i32 s2, s2, s98
	s_waitcnt lgkmcnt(0)
	v_readfirstlane_b32 s3, v3
	s_lshl_b32 s3, s3, 3
	s_cmp_lt_i32 s2, s3
	s_cselect_b64 s[30:31], -1, 0
	s_cmp_ge_i32 s2, s3
	s_cbranch_scc1 .LBB0_1035
	s_ashr_i32 s4, s2, 3
	s_lshl_b32 s3, s4, 2
	s_add_i32 s3, s77, s3
	v_mov_b32_e32 v3, s3
	ds_read_b32 v3, v3 offset:768
	s_and_b32 s96, s2, 7
	s_waitcnt lgkmcnt(0)
	v_lshlrev_b32_e32 v4, 2, v3
	v_add_u32_e32 v6, s77, v4
	ds_read2st64_b32 v[4:5], v6 offset1:1
	v_readfirstlane_b32 s2, v3
	ds_read_b32 v3, v6 offset:512
	s_ashr_i32 s3, s2, 31
	s_waitcnt lgkmcnt(0)
	v_readfirstlane_b32 s5, v5
	s_sub_i32 s4, s4, s5
	v_readfirstlane_b32 s18, v4
	s_lshl_b32 s4, s4, 8
	s_add_i32 s18, s4, s18
	s_ashr_i32 s19, s18, 31
	v_subrev_u32_e32 v3, s4, v3
	s_lshl_b64 s[4:5], s[18:19], 9
	s_add_u32 s40, s27, s4
	s_addc_u32 s41, s74, s5
	s_lshl_b64 s[2:3], s[2:3], 20
	s_add_u32 s2, s75, s2
	s_addc_u32 s3, s76, s3
	s_lshl_b32 s4, s96, 17
	v_cmp_gt_i32_e32 vcc, s91, v3
	s_add_u32 s66, s2, s4
	s_addc_u32 s67, s3, 0
	v_cndmask_b32_e64 v220, 0, 1, vcc

; #define LAS __attribute__((address_space(3)))
; DI void moe_tables(const Params& p, LAS int* MT, int layer) {
;     const int tid = threadIdx.x;
;     __syncthreads();
;     if (tid < 64) {
;         const int e = tid & 31;
;         const int c = ((const int*)(p.ws + WS_CTL + CW_CNT))[layer * NEXP + e];
;         const int t = (c + 255) >> 8;
;         int incl = t;
; #pragma unroll
;         for (int off = 1; off < 32; off <<= 1) { const int y = __shfl_up(incl, off, 32); if (e >= off) incl += y; }
;         const int tp = incl - t;
;         if (tid < 32) {
;             MT[128 + e] = c; MT[e] = tp * 256; MT[64 + e] = tp;
;             for (int k = 0; k < t; ++k) MT[192 + tp + k] = e;
;             if (e == 31) { MT[32] = incl * 256; MT[64 + 32] = incl; }
;         }
;     }
;     __syncthreads();
; }
; __global__ void __launch_bounds__(NTHREADS, 2) fwd_kernel(Params p) {
;     ...
;     if (IN(15)) for (int rep_ = 0; rep_ <= REP(15); ++rep_) { if (rep_) __syncthreads();
;         moe_tables(p, MT, 1);
;         MoeSchedUpT<true, 127 - 6> S; S.Hb = (const char*)(ws + WS_H8); S.EG = (const char*)(ws + WS_EG + EXPW); S.LIST = (const int*)(ws + WS_LIST); S.MT = MT; S.K = DM / 2;
;         S.lda = DM; S.ldb = DM; S.a_h = 0; S.b_h = WS_EU - WS_EG; S.G = G; S.c = bid; S.estride = (size_t)EFF * DM; S.wscale = 127 - 6;
.LBB0_1575:
	s_cmp_gt_i32 s24, 15
	s_cselect_b64 s[0:1], -1, 0
	s_cmp_lt_i32 s25, 16
	s_cselect_b64 s[2:3], -1, 0
	s_or_b64 s[0:1], s[0:1], s[2:3]
	s_and_b64 vcc, exec, s[0:1]
	s_cbranch_vccnz .LBB0_1734
	s_and_b32 s98, s22, 7
	s_lshl_b32 s98, s98, 5
	s_lshr_b32 s99, s22, 3
	s_or_b32 s98, s98, s99
	s_cmpk_lg_i32 s23, 0x100
	s_cselect_b32 s98, s22, s98
	s_waitcnt vmcnt(0) lgkmcnt(0)
	s_barrier
	s_and_saveexec_b64 s[0:1], s[20:21]
	s_cbranch_execz .LBB0_1593
	v_mov_b32_e32 v1, 0x80
	v_lshl_or_b32 v2, v0, 2, v1
	v_mov_b32_e32 v3, 0
	v_lshl_add_u64 v[2:3], s[50:51], 0, v[2:3]
	v_add_co_u32_e32 v2, vcc, 0x4000, v2
	v_and_b32_e32 v1, 31, v0
	s_nop 0
	v_addc_co_u32_e32 v3, vcc, 0, v3, vcc
	global_load_dword v5, v[2:3], off
	v_mbcnt_lo_u32_b32 v2, -1, 0
	v_mbcnt_hi_u32_b32 v3, -1, v2
	v_and_b32_e32 v4, 0x60, v3
	v_add_u32_e32 v2, -1, v3
	v_cmp_lt_i32_e32 vcc, v2, v4
	v_add_u32_e32 v6, -2, v3
	v_add_u32_e32 v7, -4, v3
	v_cndmask_b32_e32 v2, v2, v3, vcc
	v_lshlrev_b32_e32 v9, 2, v2
	v_cmp_lt_i32_e32 vcc, v6, v4
	v_add_u32_e32 v8, -8, v3
	s_waitcnt vmcnt(0)
	v_add_u32_e32 v2, 0xff, v5
	v_ashrrev_i32_e32 v2, 8, v2
	ds_bpermute_b32 v9, v9, v2
	v_cndmask_b32_e32 v6, v6, v3, vcc
	v_cmp_ne_u32_e32 vcc, 0, v1
	v_lshlrev_b32_e32 v6, 2, v6
	s_waitcnt lgkmcnt(0)
	v_cndmask_b32_e32 v9, 0, v9, vcc
	v_add_u32_e32 v9, v9, v2
	ds_bpermute_b32 v6, v6, v9
	v_cmp_lt_i32_e32 vcc, v7, v4
	s_nop 1
	v_cndmask_b32_e32 v7, v7, v3, vcc
	v_cmp_lt_u32_e32 vcc, 1, v1
	v_lshlrev_b32_e32 v7, 2, v7
	s_waitcnt lgkmcnt(0)
	v_cndmask_b32_e32 v6, 0, v6, vcc
	v_add_u32_e32 v6, v6, v9
	ds_bpermute_b32 v7, v7, v6
	v_cmp_lt_i32_e32 vcc, v8, v4
	s_nop 1
	v_cndmask_b32_e32 v8, v8, v3, vcc
	v_cmp_lt_u32_e32 vcc, 3, v1
	v_lshlrev_b32_e32 v8, 2, v8
	s_waitcnt lgkmcnt(0)
	v_cndmask_b32_e32 v7, 0, v7, vcc
	v_add_u32_e32 v6, v7, v6
	ds_bpermute_b32 v7, v8, v6
	v_add_u32_e32 v8, -16, v3
	v_cmp_lt_i32_e32 vcc, v8, v4
	s_nop 1
	v_cndmask_b32_e32 v4, v8, v3, vcc
	v_cmp_lt_u32_e32 vcc, 7, v1
	v_lshlrev_b32_e32 v4, 2, v4
	s_waitcnt lgkmcnt(0)
	v_cndmask_b32_e32 v3, 0, v7, vcc
	v_add_u32_e32 v3, v3, v6
	ds_bpermute_b32 v4, v4, v3
	v_cmp_gt_u32_e32 vcc, 32, v0
	s_and_b64 exec, exec, vcc
	s_cbranch_execz .LBB0_1593
	v_cmp_lt_u32_e32 vcc, 15, v1
	s_add_i32 s2, 0, 0x22040
	v_lshl_add_u32 v7, v1, 2, s2
	s_waitcnt lgkmcnt(0)
	v_cndmask_b32_e32 v4, 0, v4, vcc
	v_add_u32_e32 v3, v4, v3
	v_sub_u32_e32 v4, v3, v2
	v_lshlrev_b32_e32 v8, 8, v4
	v_cmp_lt_i32_e32 vcc, 0, v2
	v_lshl_add_u32 v6, v0, 2, s2
	ds_write_b32 v7, v8
	ds_write2st64_b32 v6, v4, v5 offset0:1 offset1:2
	s_and_saveexec_b64 s[2:3], vcc
	s_cbranch_execz .LBB0_1591
	v_cmp_ne_u32_e32 vcc, 1, v2
	s_mov_b64 s[6:7], -1
	v_mov_b32_e32 v5, 0
	s_and_saveexec_b64 s[4:5], vcc
	s_cbranch_execz .LBB0_1588
	v_add_u32_e32 v6, -2, v2
	v_lshrrev_b32_e32 v5, 1, v6
	v_add_u32_e32 v5, 1, v5
	v_cmp_lt_u32_e32 vcc, 13, v6
	v_mov_b32_e32 v8, 0
	s_and_saveexec_b64 s[6:7], vcc
	s_cbranch_execz .LBB0_1584
	v_lshl_add_u32 v7, v4, 2, 0
	v_and_b32_e32 v6, -8, v5
	s_mov_b32 s10, 0
	v_add_u32_e32 v7, 0x22340, v7
	s_mov_b64 s[8:9], 0

;     DI bool next(int i, pg8::GU& u) const { int pm, pn; if (!T.tile(i, pm, pn)) return false; u.pm = pm; u.pn = pn; u.e = 0; u.aux = 0; u.h1 = 0; u.a = A + (size_t)pm * 256 * lda; u.b = Bt + (size_t)pn * 256 * ldb; return true; }
;     DI bool next(int i, pg8::GU& u) const {
;         const int L = i * G + c, T = MT[64 + 32]; if (L >= T * 4) return false;
;         const int rt = L >> 2, ct = L & 3; const int e = MT[192 + rt];
;         const int lt = rt - MT[64 + e];
;         u.e = e; u.pm = lt; u.pn = ct; u.aux = MT[e] + 256 * lt; u.h1 = (MT[128 + e] - 256 * lt) <= 128; u.a = Hb; u.b = EG + (size_t)e * estride + (size_t)ct * 128 * ldb; return true;
.LBB0_1593:
	s_or_b64 exec, exec, s[0:1]
	s_add_u32 s0, s50, 0x41b76000
	s_addc_u32 s1, s51, 0
	s_add_u32 s52, s50, 0x710e000
	s_addc_u32 s53, s51, 0
	s_add_i32 s2, 0, 0x221c0
	v_mov_b32_e32 v1, s2
	s_waitcnt lgkmcnt(0)
	s_barrier
	ds_read_b32 v1, v1
	s_and_b32 s84, s98, 3
	v_lshrrev_b32_e32 v2, 3, v0
	v_readfirstlane_b32 s8, v0
	s_waitcnt lgkmcnt(0)
	v_readfirstlane_b32 s2, v1
	s_lshl_b32 s9, s2, 2
	s_cmp_lt_i32 s98, s9
	s_cselect_b64 s[6:7], -1, 0
	s_cmp_ge_i32 s98, s9
	s_mov_b32 s2, 0
	s_cbranch_scc1 .LBB0_1595
	s_and_b32 s2, s98, -4
	s_add_i32 s3, 0, 0x22040
	s_add_i32 s2, s3, s2
	v_mov_b32_e32 v1, s2
	ds_read_b32 v3, v1 offset:768
	s_lshr_b32 s2, s98, 2
	s_lshl_b32 s4, s84, 18
	s_add_u32 s10, s52, s4
	s_mov_b64 s[34:35], s[0:1]
	s_waitcnt lgkmcnt(0)
	v_lshlrev_b32_e32 v1, 2, v3
	v_add_u32_e32 v1, s3, v1
	ds_read2st64_b32 v[4:5], v1 offset1:1
	ds_read_b32 v1, v1 offset:512
	s_addc_u32 s3, s53, 0
	v_readfirstlane_b32 s4, v3
	s_ashr_i32 s5, s4, 31
	s_waitcnt lgkmcnt(1)
	v_readfirstlane_b32 s11, v5
	s_sub_i32 s2, s2, s11
	s_lshl_b32 s2, s2, 8
	s_waitcnt lgkmcnt(0)
	v_subrev_u32_e32 v1, s2, v1
	s_movk_i32 s11, 0x81
	s_lshl_b64 s[4:5], s[4:5], 20
	v_cmp_gt_i32_e32 vcc, s11, v1
	s_add_u32 s4, s10, s4
	v_add_u32_e32 v239, s2, v4
	v_cndmask_b32_e64 v10, 0, 1, vcc
	s_addc_u32 s5, s3, s5
	s_branch .LBB0_1596

;     DI bool next(int i, pg8::GU& u) const { int pm, pn; if (!T.tile(i, pm, pn)) return false; u.pm = pm; u.pn = pn; u.e = 0; u.aux = 0; u.h1 = 0; u.a = A + (size_t)pm * 256 * lda; u.b = Bt + (size_t)pn * 256 * ldb; return true; }
;     DI bool next(int i, pg8::GU& u) const {
;         const int L = i * G + c, T = MT[64 + 32]; if (L >= T * 4) return false;
;         const int rt = L >> 2, ct = L & 3; const int e = MT[192 + rt];
;         const int lt = rt - MT[64 + e];
;         u.e = e; u.pm = lt; u.pn = ct; u.aux = MT[e] + 256 * lt; u.h1 = (MT[128 + e] - 256 * lt) <= 128; u.a = Hb; u.b = EG + (size_t)e * estride + (size_t)ct * 128 * ldb; return true;
.LBB0_1610:
	ds_read_b32 v2, v226
	s_add_i32 s62, s62, 1
	s_mul_i32 s2, s62, s23
	s_add_i32 s2, s2, s98
	s_waitcnt lgkmcnt(0)
	v_readfirstlane_b32 s3, v2
	s_lshl_b32 s3, s3, 2
	s_cmp_lt_i32 s2, s3
	s_cselect_b64 s[6:7], -1, 0
	s_cmp_ge_i32 s2, s3
	s_cbranch_scc1 .LBB0_1612
	s_and_b32 s3, s2, -4
	s_add_i32 s3, s76, s3
	v_mov_b32_e32 v2, s3
	ds_read_b32 v232, v2 offset:768
	s_ashr_i32 s8, s2, 2
	s_and_b32 s82, s2, 3
	s_mov_b64 s[30:31], s[0:1]
	s_waitcnt lgkmcnt(0)
	v_lshlrev_b32_e32 v2, 2, v232
	v_add_u32_e32 v4, s76, v2
	ds_read2st64_b32 v[2:3], v4 offset1:1
	ds_read_b32 v4, v4 offset:512
	v_readfirstlane_b32 s2, v232
	s_ashr_i32 s3, s2, 31
	s_lshl_b64 s[2:3], s[2:3], 20
	s_waitcnt lgkmcnt(0)
	v_readfirstlane_b32 s9, v3
	s_sub_i32 s83, s8, s9
	s_lshl_b32 s8, s83, 8
	s_add_u32 s2, s52, s2
	v_add_u32_e32 v233, s8, v2
	v_subrev_u32_e32 v2, s8, v4
	s_addc_u32 s3, s53, s3
	s_lshl_b32 s8, s82, 18
	v_cmp_gt_i32_e32 vcc, s77, v2
	s_add_u32 s26, s2, s8
	s_addc_u32 s27, s3, 0
	v_cndmask_b32_e64 v234, 0, 1, vcc

; DI void cvt_group(const Params& p, LAS unsigned char* lds, int group, int t_lo, int t_hi, int r, int I) {
;     ...
;     if (tid == 0) {
;         int t0 = 0, nj = 0;
;         if (group == 0) {
;             set_job(J, 0, p.in[11], (bf16_t*)(ws + WS_W0IN), DM, L0IN, DM, 0, 1, 0, 0, t0);
;             set_job(J, 1, p.in[13], (bf16_t*)(ws + WS_WUQ), 512, 1536, 512, 0, 1, 0, 0, t0);
;             set_job(J, 2, p.in[15], (bf16_t*)(ws + WS_WUKV), 256, 2048, 256, 0, 1, 0, 0, t0);
;             set_job(J, 3, p.in[23], (bf16_t*)(ws + WS_W0OUT), DM, DM, DM, 0, 1, 0, 0, t0);
;             set_job(J, 4, p.in[31], (bf16_t*)(ws + WS_W1IN), DM, L1IN, DM, 1, 1, 0, 0, t0); if (FP8_IN1) J[4].f8scale = 64.f;
;             set_job(J, 5, p.in[34], (bf16_t*)(ws + WS_W1OUT), DM, DM, DM, 0, 1, 0, 0, t0); if (FP8_OUT1) J[5].f8scale = 64.f;
;             set_job(J, 6, p.in[18], (bf16_t*)(ws + WS_GW), 128, 128, 128, 0, 16, 128 * 128, 128 * 128, t0);
;             set_job(J, 7, p.in[20], (bf16_t*)(ws + WS_GW + (size_t)16 * 128 * 128 * 2), 128, 128, 128, 0, 16, 128 * 128, 128 * 128, t0);
;             nj = 8;
;         } else if (group == 1) {
;             set_job(J, 0, p.in[24], (bf16_t*)(ws + WS_EG), DM, EFF, DM, 0, NEXP, (size_t)DM * EFF, (size_t)EFF * DM, t0);
;             set_job(J, 1, p.in[25], (bf16_t*)(ws + WS_EU), DM, EFF, DM, 0, NEXP, (size_t)DM * EFF, (size_t)EFF * DM, t0);
;             set_job(J, 2, p.in[26], (bf16_t*)(ws + WS_ED), EFF, DM, EFF, 0, NEXP, (size_t)DM * EFF, (size_t)EFF * DM, t0);
;             if (FP8_L0) { J[0].f8scale = 64.f; J[1].f8scale = 64.f; J[2].f8scale = 32.f; }
;             nj = 3;
;         } else {
;             set_job(J, 0, p.in[35], (bf16_t*)(ws + WS_EG + EXPW), DM, EFF, DM, 0, NEXP, (size_t)DM * EFF, (size_t)EFF * DM, t0); J[0].f8scale = 64.f;
;             set_job(J, 1, p.in[36], (bf16_t*)(ws + WS_EU + EXPW), DM, EFF, DM, 0, NEXP, (size_t)DM * EFF, (size_t)EFF * DM, t0); J[1].f8scale = 64.f;
;             set_job(J, 2, p.in[37], (bf16_t*)(ws + WS_ED + EXPW), EFF, DM, EFF, 0, NEXP, (size_t)DM * EFF, (size_t)EFF * DM, t0); J[2].f8scale = 32.f;
;             nj = 3;
;         }
;         J[nj].tile0 = t0; J[15].tile0 = nj;
;     }
;     __syncthreads();
;     const int nj = J[15].tile0, total = J[nj].tile0;
;     const int hi = min(t_hi, total);
;     const int row = tid >> 6, c4 = (tid & 63) * 4;
;     for (int gt = t_lo + r; gt < hi; gt += I) {
.LBB0_1640:
	s_add_u32 s16, s50, 0xf10e000
	s_addc_u32 s17, s51, 0
	s_add_u32 s14, s50, 0x1710e000
	s_addc_u32 s15, s51, 0
	s_abs_i32 s0, s23
	v_cvt_f32_u32_e32 v3, s0
	s_sub_i32 s5, 0, s0
	s_abs_i32 s4, s9
	s_ashr_i32 s1, s9, 31
	v_rcp_iflag_f32_e32 v3, v3
	v_and_b32_e32 v11, 0xff, v0
	v_lshlrev_b32_e32 v4, 1, v0
	v_mul_u32_u24_e32 v2, 0x410, v198
	v_mul_f32_e32 v3, 0x4f7ffffe, v3
	v_cvt_u32_f32_e32 v3, v3
	v_and_b32_e32 v10, 0xfc, v199
	v_and_b32_e32 v4, 32, v4
	v_lshl_add_u32 v16, v11, 2, 0
	v_readfirstlane_b32 s6, v3
	s_mul_i32 s5, s5, s6
	s_mul_hi_u32 s5, s6, s5
	s_add_i32 s6, s6, s5
	s_mul_hi_u32 s5, s4, s6
	s_mul_i32 s5, s5, s0
	s_sub_i32 s4, s4, s5
	s_sub_i32 s5, s4, s0
	s_cmp_ge_u32 s4, s0
	s_cselect_b32 s4, s5, s4
	s_sub_i32 s5, s4, s0
	s_cmp_ge_u32 s4, s0
	s_cselect_b32 s0, s5, s4
	s_xor_b32 s0, s0, s1
	s_sub_i32 s4, s0, s1
	v_mul_u32_u24_e32 v14, 0x410, v222
	v_mul_u32_u24_e32 v13, 0x410, v223
	v_cmp_eq_u32_e64 s[2:3], 0, v0
	v_mov_b32_e32 v199, 0
	v_lshl_add_u32 v15, v10, 2, 0
	v_and_or_b32 v1, v1, 16, v4
	s_cmp_lg_u32 s4, 0
	v_add_u32_e32 v12, v16, v2
	s_cbranch_scc0 .LBB0_1663
	s_cmp_lt_i32 s98, s4
	s_cbranch_scc1 .LBB0_1662
	s_waitcnt vmcnt(0)
	s_barrier
	s_and_saveexec_b64 s[0:1], s[2:3]
	s_cbranch_execz .LBB0_1644
	s_movk_i32 s8, 0x800
	s_mov_b32 s11, 0
	s_add_i32 s5, 0, 0x12000
	s_mov_b32 s10, s8
	v_mov_b32_e32 v2, s42
	v_mov_b32_e32 v3, s43
	v_mov_b32_e32 v4, s52
	v_mov_b32_e32 v5, s53
	v_mov_b32_e32 v6, s5
	s_movk_i32 s9, 0x200
	s_add_i32 s5, 0, 0x12010
	v_mov_b64_e32 v[24:25], s[10:11]
	ds_write_b128 v6, v[2:5]
	v_mov_b32_e32 v2, s5
	v_mov_b64_e32 v[22:23], s[8:9]
	s_add_i32 s5, 0, 0x12020
	s_mov_b32 s6, 0x100000
	ds_write_b128 v2, v[22:25]
	v_mov_b32_e32 v8, 64
	v_mov_b32_e32 v9, 0
	v_mov_b32_e32 v2, s5
	s_add_i32 s5, 0, 0x12028
	s_mov_b32 s7, s11
	s_mov_b32 s10, s6
	ds_write_b64 v2, v[8:9]
	v_mov_b32_e32 v2, s5
	v_mov_b64_e32 v[18:19], s[6:7]
	v_mov_b64_e32 v[20:21], s[10:11]
	s_add_i32 s5, 0, 0x12040
	ds_write2_b64 v2, v[18:19], v[20:21] offset1:1
	v_mov_b32_e32 v2, s44
	v_mov_b32_e32 v3, s45
	v_mov_b32_e32 v4, s16
	v_mov_b32_e32 v5, s17
	v_mov_b32_e32 v6, s5
	s_add_i32 s5, 0, 0x12050
	ds_write_b128 v6, v[2:5]
	v_mov_b32_e32 v2, s5
	s_add_i32 s5, 0, 0x12060
	ds_write_b128 v2, v[22:25]
	v_mov_b32_e32 v3, 0x800
	v_mov_b32_e32 v2, v8
	v_mov_b32_e32 v4, s5
	s_add_i32 s5, 0, 0x12068
	ds_write_b64 v4, v[2:3]
	v_mov_b32_e32 v2, s5
	s_add_i32 s5, 0, 0x12080
	ds_write2_b64 v2, v[18:19], v[20:21] offset1:1
	v_mov_b32_e32 v4, s46
	v_mov_b32_e32 v5, s47
	v_mov_b32_e32 v6, s14
	v_mov_b32_e32 v7, s15
	v_mov_b32_e32 v2, s5
	ds_write_b128 v2, v[4:7]
	v_mov_b32_e32 v2, 0x200
	s_add_i32 s5, 0, 0x12090
	v_mov_b32_e32 v4, v2
	v_mov_b32_e32 v5, v9
	v_mov_b32_e32 v6, s5
	s_add_i32 s5, 0, 0x120a0
	ds_write_b128 v6, v[2:5]
	v_mov_b32_e32 v9, 0x1000
	v_mov_b32_e32 v2, s5
	s_add_i32 s5, 0, 0x120a8
	ds_write_b64 v2, v[8:9]
	v_mov_b32_e32 v2, s5
	s_add_i32 s5, 0, 0x12038
	ds_write2_b64 v2, v[18:19], v[20:21] offset1:1
	v_mov_b32_e32 v2, 0x42800000
	v_mov_b32_e32 v3, s5
	s_add_i32 s5, 0, 0x12078
	ds_write_b32 v3, v2
	v_mov_b32_e32 v3, s5
	s_add_i32 s5, 0, 0x120b8
	ds_write_b32 v3, v2
	v_mov_b32_e32 v2, 0x42000000
	v_mov_b32_e32 v3, s5
	s_add_i32 s5, 0, 0x120e4
	ds_write_b32 v3, v2
	v_mov_b32_e32 v2, 0x1800
	v_mov_b32_e32 v3, s5
	s_add_i32 s5, 0, 0x123e4
	ds_write_b32 v3, v2
	v_mov_b32_e32 v2, 3
	v_mov_b32_e32 v3, s5
	ds_write_b32 v3, v2
.LBB0_1644:
	s_or_b64 exec, exec, s[0:1]
	s_add_i32 s0, 0, 0x123e4
	v_mov_b32_e32 v2, s0
	s_waitcnt lgkmcnt(0)
	s_barrier
	ds_read_b32 v2, v2
	s_sub_i32 s0, s98, s4
	s_add_i32 s18, s0, 0x1000
	s_waitcnt lgkmcnt(0)
	v_lshlrev_b32_e32 v3, 6, v2
	v_add_u32_e32 v3, 0, v3
	v_add_u32_e32 v3, 0x12024, v3
	ds_read_b32 v3, v3
	v_readfirstlane_b32 s19, v2
	s_waitcnt lgkmcnt(0)
	v_min_i32_e32 v17, 0x1800, v3
	v_cmp_ge_i32_e32 vcc, s18, v17
	s_cbranch_vccnz .LBB0_1662
	s_sub_i32 s26, s23, s4
	s_cmp_gt_i32 s19, 1
	s_cselect_b64 s[0:1], -1, 0
	s_add_i32 s4, s19, -1
	s_cmp_lg_u32 s19, 2
	v_cndmask_b32_e64 v2, 0, 1, s[0:1]
	s_cselect_b64 s[0:1], -1, 0
	s_and_b32 s27, s4, -2
	s_or_b32 s30, s4, 1
	s_cmp_lg_u32 s4, s27
	v_cndmask_b32_e64 v4, 0, 1, s[0:1]
	s_cselect_b64 s[8:9], -1, 0
	v_cmp_ne_u32_e64 s[4:5], 1, v2
	s_add_i32 s31, 0, 0x120a4
	s_brev_b32 s34, 1
	v_lshlrev_b32_e32 v2, 2, v10
	v_mov_b32_e32 v3, 0
	v_add_u32_e32 v18, v15, v14
	s_movk_i32 s35, 0x4ff
	s_movk_i32 s36, 0xffcf
	s_mov_b32 s37, 0xc3e00000
	v_cmp_ne_u32_e64 s[6:7], 1, v4
	v_mov_b32_e32 v19, 0x43e00000
	s_branch .LBB0_1648

; #define LAS __attribute__((address_space(3)))
; DI void cvt_group(const Params& p, LAS unsigned char* lds, int group, int t_lo, int t_hi, int r, int I) {
;     ...
;     __syncthreads();
;     const int nj = J[15].tile0, total = J[nj].tile0;
;     const int hi = min(t_hi, total);
;     const int row = tid >> 6, c4 = (tid & 63) * 4;
;     for (int gt = t_lo + r; gt < hi; gt += I) {
;         CvtTile cur; cvt_decode(J, nj, gt, cur);
; DI void bg_range(const Params& p, LAS unsigned char* lds, int group, int t_lo, int t_hi, int nunits, int G, int bid) {
;     const int rem = nunits % G;
;     if (rem == 0) cvt_group(p, lds, group, t_lo, t_hi, bid, G);
;     else if (bid >= rem) cvt_group(p, lds, group, t_lo, t_hi, bid - rem, G - rem);
.LBB0_1666:
	s_or_b64 exec, exec, s[0:1]
	s_add_i32 s0, 0, 0x123e4
	v_mov_b32_e32 v2, s0
	s_waitcnt lgkmcnt(0)
	s_barrier
	ds_read_b32 v2, v2
	s_add_i32 s14, s98, 0x1000
	s_waitcnt lgkmcnt(0)
	v_lshlrev_b32_e32 v3, 6, v2
	v_add_u32_e32 v3, 0, v3
	v_add_u32_e32 v3, 0x12024, v3
	ds_read_b32 v3, v3
	v_readfirstlane_b32 s16, v2
	s_waitcnt lgkmcnt(0)
	v_readfirstlane_b32 s0, v3
	s_min_i32 s15, s0, 0x1800
	s_cmp_ge_i32 s14, s15
	s_cbranch_scc1 .LBB0_1684
	s_cmp_gt_i32 s16, 1
	s_cselect_b64 s[0:1], -1, 0
	s_add_i32 s4, s16, -1
	s_cmp_lg_u32 s16, 2
	v_cndmask_b32_e64 v2, 0, 1, s[0:1]
	s_cselect_b64 s[0:1], -1, 0
	s_and_b32 s17, s4, -2
	s_or_b32 s18, s4, 1
	s_cmp_lg_u32 s4, s17
	v_cndmask_b32_e64 v4, 0, 1, s[0:1]
	s_cselect_b64 s[8:9], -1, 0
	v_cmp_ne_u32_e64 s[4:5], 1, v2
	s_add_i32 s19, 0, 0x120a4
	s_brev_b32 s26, 1
	v_lshlrev_b32_e32 v2, 2, v10
	v_mov_b32_e32 v3, 0
	v_add_u32_e32 v14, v15, v14
	s_movk_i32 s27, 0x4ff
	s_movk_i32 s30, 0xffcf
	s_mov_b32 s31, 0xc3e00000
	v_cmp_ne_u32_e64 s[6:7], 1, v4
	v_add_u32_e32 v13, v16, v13
	v_mov_b32_e32 v15, 0x43e00000
	s_branch .LBB0_1670

; #define LAS __attribute__((address_space(3)))
; DI void moe_tables(const Params& p, LAS int* MT, int layer) {
;     const int tid = threadIdx.x;
;     __syncthreads();
;     if (tid < 64) {
;         const int e = tid & 31;
;         const int c = ((const int*)(p.ws + WS_CTL + CW_CNT))[layer * NEXP + e];
;         const int t = (c + 255) >> 8;
;         int incl = t;
; #pragma unroll
;         for (int off = 1; off < 32; off <<= 1) { const int y = __shfl_up(incl, off, 32); if (e >= off) incl += y; }
;         const int tp = incl - t;
;         if (tid < 32) {
;             MT[128 + e] = c; MT[e] = tp * 256; MT[64 + e] = tp;
;             for (int k = 0; k < t; ++k) MT[192 + tp + k] = e;
;             if (e == 31) { MT[32] = incl * 256; MT[64 + 32] = incl; }
;         }
;     }
;     __syncthreads();
; }
; __global__ void __launch_bounds__(NTHREADS, 2) fwd_kernel(Params p) {
;     ...
;     if (IN(16)) for (int rep_ = 0; rep_ <= REP(16); ++rep_) { if (rep_) __syncthreads();
;         moe_tables(p, MT, 1);
;         MoeSchedDownT<true, 127 - 5> S; S.ACT = (const char*)(ws + WS_ACT); S.ED = (const char*)(ws + WS_ED + EXPW); S.MT = MT; S.K = EFF / 2;
;         S.lda = EFF; S.ldb = EFF; S.a_h = 128 * EFF; S.b_h = 128 * EFF; S.G = G; S.c = bid; S.estride = (size_t)DM * EFF; S.wscale = 127 - 5;
.LBB0_1734:
	s_cmp_gt_i32 s24, 16
	s_cselect_b64 s[0:1], -1, 0
	s_cmp_lt_i32 s25, 17
	s_cselect_b64 s[2:3], -1, 0
	s_or_b64 s[0:1], s[0:1], s[2:3]
	s_and_b64 vcc, exec, s[0:1]
	s_cbranch_vccnz .LBB0_1828
	s_and_b32 s98, s22, 7
	s_lshl_b32 s98, s98, 5
	s_lshr_b32 s99, s22, 3
	s_or_b32 s98, s98, s99
	s_cmpk_lg_i32 s23, 0x100
	s_cselect_b32 s98, s22, s98
	s_waitcnt vmcnt(0) lgkmcnt(0)
	s_barrier
	s_and_saveexec_b64 s[0:1], s[20:21]
	s_cbranch_execz .LBB0_1752
	v_mov_b32_e32 v1, 0x80
	v_lshl_or_b32 v2, v0, 2, v1
	v_mov_b32_e32 v3, 0
	v_lshl_add_u64 v[2:3], s[50:51], 0, v[2:3]
	v_add_co_u32_e32 v2, vcc, 0x4000, v2
	v_and_b32_e32 v1, 31, v0
	s_nop 0
	v_addc_co_u32_e32 v3, vcc, 0, v3, vcc
	global_load_dword v5, v[2:3], off
	v_mbcnt_lo_u32_b32 v2, -1, 0
	v_mbcnt_hi_u32_b32 v3, -1, v2
	v_and_b32_e32 v4, 0x60, v3
	v_add_u32_e32 v2, -1, v3
	v_cmp_lt_i32_e32 vcc, v2, v4
	v_add_u32_e32 v6, -2, v3
	v_add_u32_e32 v7, -4, v3
	v_cndmask_b32_e32 v2, v2, v3, vcc
	v_lshlrev_b32_e32 v9, 2, v2
	v_cmp_lt_i32_e32 vcc, v6, v4
	v_add_u32_e32 v8, -8, v3
	s_waitcnt vmcnt(0)
	v_add_u32_e32 v2, 0xff, v5
	v_ashrrev_i32_e32 v2, 8, v2
	ds_bpermute_b32 v9, v9, v2
	v_cndmask_b32_e32 v6, v6, v3, vcc
	v_cmp_ne_u32_e32 vcc, 0, v1
	v_lshlrev_b32_e32 v6, 2, v6
	s_waitcnt lgkmcnt(0)
	v_cndmask_b32_e32 v9, 0, v9, vcc
	v_add_u32_e32 v9, v9, v2
	ds_bpermute_b32 v6, v6, v9
	v_cmp_lt_i32_e32 vcc, v7, v4
	s_nop 1
	v_cndmask_b32_e32 v7, v7, v3, vcc
	v_cmp_lt_u32_e32 vcc, 1, v1
	v_lshlrev_b32_e32 v7, 2, v7
	s_waitcnt lgkmcnt(0)
	v_cndmask_b32_e32 v6, 0, v6, vcc
	v_add_u32_e32 v6, v6, v9
	ds_bpermute_b32 v7, v7, v6
	v_cmp_lt_i32_e32 vcc, v8, v4
	s_nop 1
	v_cndmask_b32_e32 v8, v8, v3, vcc
	v_cmp_lt_u32_e32 vcc, 3, v1
	v_lshlrev_b32_e32 v8, 2, v8
	s_waitcnt lgkmcnt(0)
	v_cndmask_b32_e32 v7, 0, v7, vcc
	v_add_u32_e32 v6, v7, v6
	ds_bpermute_b32 v7, v8, v6
	v_add_u32_e32 v8, -16, v3
	v_cmp_lt_i32_e32 vcc, v8, v4
	s_nop 1
	v_cndmask_b32_e32 v4, v8, v3, vcc
	v_cmp_lt_u32_e32 vcc, 7, v1
	v_lshlrev_b32_e32 v4, 2, v4
	s_waitcnt lgkmcnt(0)
	v_cndmask_b32_e32 v3, 0, v7, vcc
	v_add_u32_e32 v3, v3, v6
	ds_bpermute_b32 v4, v4, v3
	v_cmp_gt_u32_e32 vcc, 32, v0
	s_and_b64 exec, exec, vcc
	s_cbranch_execz .LBB0_1752
	v_cmp_lt_u32_e32 vcc, 15, v1
	s_add_i32 s2, 0, 0x22040
	v_lshl_add_u32 v7, v1, 2, s2
	s_waitcnt lgkmcnt(0)
	v_cndmask_b32_e32 v4, 0, v4, vcc
	v_add_u32_e32 v3, v4, v3
	v_sub_u32_e32 v4, v3, v2
	v_lshlrev_b32_e32 v8, 8, v4
	v_cmp_lt_i32_e32 vcc, 0, v2
	v_lshl_add_u32 v6, v0, 2, s2
	ds_write_b32 v7, v8
	ds_write2st64_b32 v6, v4, v5 offset0:1 offset1:2
	s_and_saveexec_b64 s[2:3], vcc
	s_cbranch_execz .LBB0_1750
	v_cmp_ne_u32_e32 vcc, 1, v2
	s_mov_b64 s[6:7], -1
	v_mov_b32_e32 v5, 0
	s_and_saveexec_b64 s[4:5], vcc
	s_cbranch_execz .LBB0_1747
	v_add_u32_e32 v6, -2, v2
	v_lshrrev_b32_e32 v5, 1, v6
	v_add_u32_e32 v5, 1, v5
	v_cmp_lt_u32_e32 vcc, 13, v6
	v_mov_b32_e32 v8, 0
	s_and_saveexec_b64 s[6:7], vcc
	s_cbranch_execz .LBB0_1743
	v_lshl_add_u32 v7, v4, 2, 0
	v_and_b32_e32 v6, -8, v5
	s_mov_b32 s10, 0
	v_add_u32_e32 v7, 0x22340, v7
	s_mov_b64 s[8:9], 0

; #define PG8_STAGE_A(bufoff, gbase, h, VG) do { if constexpr (Sched::GATHER) { PG8_STAGE(bufoff, gbase, VG[h]); } else { PG8_STAGE(bufoff, (gbase) + (h) * ahs, voffA); } } while (0)
; #define PG8_STAGE_B(bufoff, gbase, h) PG8_STAGE(bufoff, (gbase) + (h) * bhs, voffB)
; #define PG8_WAIT_V(n) asm volatile("s_waitcnt vmcnt(" #n ")" ::: "memory")
; #define PG8_BAR __builtin_amdgcn_s_barrier()
;     DI unsigned rowoff(const pg8::GU& u, int r) const { const int gr = 256 * u.pm + r; const int tok = gr < MT[128 + u.e] ? LIST[(size_t)u.e * MOE_CAP + gr] : NTOK; return (unsigned)tok * (unsigned)lda; }
;     DI bool next(int i, pg8::GU& u) const { int pm, pn; if (!T.tile(i, pm, pn)) return false; u.pm = pm; u.pn = pn; u.e = 0; u.aux = 0; u.h1 = 0; u.a = A + (size_t)pm * 256 * lda; u.b = Bt + (size_t)pn * 256 * ldb; return true; }
; template <class Epi, class Sched>
; DI void gemm_phase(LAS unsigned char* lds, const Sched& S, const Epi& E) {
;     ...
;     if constexpr (Sched::GATHER) {
; #pragma unroll
;         for (int h = 0; h < 2; ++h)
; #pragma unroll
;             for (int i = 0; i < 2; ++i) { vc[h][i] = S.rowoff(cur, RR[i] + 128 * h) + (unsigned)(CC[i] * 2); vn[h][i] = vc[h][i]; }
;     } else {
; #pragma unroll
;         for (int h = 0; h < 2; ++h)
; #pragma unroll
;             for (int i = 0; i < 2; ++i) { vc[h][i] = 0u; vn[h][i] = 0u; }
;     }
;     const char* cA = cur.a; const char* cB = cur.b;
;     if constexpr (PG8_SP2) {
;         PG8_STAGE_B(PG8_SB(0, 0), cB, 0); PG8_STAGE_B(PG8_SB(0, 1), cB, 1); PG8_STAGE_A(PG8_SA(0, 0), cA, 0, vc); PG8_STAGE_A(PG8_SA(0, 1), cA, 1, vc);
;         if (wr == 1) PG8_BAR;
;         PG8_WAIT_V(2); PG8_BAR;
;         PG8_STAGE_B(PG8_SB(1, 0), cB + kstep, 0); PG8_STAGE_A(PG8_SA(1, 0), cA + kstep, 0, vc); PG8_STAGE_B(PG8_SB(1, 1), cB + kstep, 1);
;         PG8_WAIT_V(6); PG8_BAR;
;     DI bool next(int i, pg8::GU& u) const {
;         const int L = i * G + c, T = MT[64 + 32]; if (L >= T * 8) return false;
;         const int rt = L >> 3, ct = L & 7; const int e = MT[192 + rt];
;         const int lt = rt - MT[64 + e];
;         u.e = e; u.pm = lt; u.pn = ct; u.aux = MT[e] + 256 * lt; u.h1 = (MT[128 + e] - 256 * lt) <= 128; u.a = ACT + (size_t)u.aux * lda; u.b = ED + (size_t)e * estride + (size_t)ct * 256 * ldb; return true;
.LBB0_1752:
	s_or_b64 exec, exec, s[0:1]
	s_add_i32 s0, 0, 0x221c0
	v_mov_b32_e32 v1, s0
	s_waitcnt lgkmcnt(0)
	s_barrier
	ds_read_b32 v1, v1
	v_readfirstlane_b32 s2, v0
	s_waitcnt lgkmcnt(0)
	v_lshlrev_b32_e32 v1, 3, v1
	v_cmp_ge_i32_e32 vcc, s98, v1
	s_cbranch_vccnz .LBB0_1778
	v_lshrrev_b32_e32 v1, 5, v0
	v_lshrrev_b32_e32 v3, 1, v0
	s_lshr_b32 s4, s2, 6
	v_and_b32_e32 v1, 4, v1
	v_bfe_u32 v2, v0, 2, 2
	v_and_b32_e32 v10, 24, v3
	s_lshr_b32 s3, s2, 8
	s_lshl_b32 s8, s4, 10
	v_or3_b32 v1, v1, v2, v10
	v_lshlrev_b32_e32 v2, 4, v0
	v_bfe_u32 v3, v0, 3, 25
	v_and_b32_e32 v5, 32, v0
	s_add_u32 s60, s50, 0x32d76000
	v_or_b32_e32 v3, 64, v3
	s_movk_i32 s0, 0x60
	v_bitop3_b32 v2, v2, v5, 48 bitop3:0x6c
	s_addc_u32 s61, s51, 0
	v_and_or_b32 v4, v3, s0, v1
	v_and_or_b32 v2, v0, 64, v2
	s_add_u32 s62, s50, 0x1710e000
	v_lshl_or_b32 v198, v4, 9, v2
	v_bfe_u32 v4, v0, 2, 4
	s_movk_i32 s0, 0x70
	s_addc_u32 s63, s51, 0
	v_and_or_b32 v3, v3, s0, v4
	s_ashr_i32 s5, s98, 3
	v_lshl_or_b32 v200, v3, 9, v2
	v_lshrrev_b32_e32 v3, 3, v0
	s_add_i32 s66, 0, 0x22040
	s_lshl_b32 s0, s5, 2
	v_and_or_b32 v1, v3, 32, v1
	s_add_i32 s0, s66, s0
	v_lshl_or_b32 v202, v1, 9, v2
	v_and_or_b32 v1, v3, 48, v4
	v_mov_b32_e32 v3, s0
	ds_read_b32 v4, v3 offset:768
	v_lshl_or_b32 v204, v1, 9, v2
	s_and_b32 s89, s98, 7
	s_lshl_b32 s0, s89, 17
	s_add_u32 s9, s62, s0
	s_waitcnt lgkmcnt(0)
	v_lshlrev_b32_e32 v1, 2, v4
	v_add_u32_e32 v1, s66, v1
	ds_read2st64_b32 v[2:3], v1 offset1:1
	s_addc_u32 s10, s63, 0
	v_readfirstlane_b32 s0, v4
	s_ashr_i32 s1, s0, 31
	ds_read_b32 v1, v1 offset:512
	s_waitcnt lgkmcnt(1)
	v_readfirstlane_b32 s6, v3
	s_sub_i32 s5, s5, s6
	s_lshl_b32 s5, s5, 8
	v_readfirstlane_b32 s6, v2
	s_add_i32 s42, s5, s6
	s_ashr_i32 s43, s42, 31
	s_lshl_b64 s[6:7], s[42:43], 9
	s_add_u32 s46, s60, s6
	s_addc_u32 s47, s61, s7
	s_lshl_b64 s[0:1], s[0:1], 20
	s_add_u32 s52, s9, s0
	s_addc_u32 s53, s10, s1
	s_add_i32 s43, s8, 0
	s_add_i32 s67, s43, 0x10000
	s_add_i32 s68, s43, 0x12000
	s_mov_b32 m0, s67
	s_add_u32 s0, s52, 0x10000
	global_load_lds_dwordx4 v202, s[52:53]
	s_mov_b32 m0, s68
	s_addc_u32 s1, s53, 0
	s_add_i32 s69, s43, 0x14000
	global_load_lds_dwordx4 v198, s[52:53]
	s_mov_b32 m0, s69
	s_add_i32 s70, s43, 0x16000
	global_load_lds_dwordx4 v202, s[0:1]
	s_mov_b32 m0, s70
	s_add_i32 s71, s43, 0x2000
	global_load_lds_dwordx4 v198, s[0:1]
	s_mov_b32 m0, s43
	s_add_u32 s0, s46, 0x10000
	global_load_lds_dwordx4 v204, s[46:47]
	s_mov_b32 m0, s71
	s_addc_u32 s1, s47, 0
	s_add_i32 s72, s43, 0x4000
	global_load_lds_dwordx4 v200, s[46:47]
	s_mov_b32 m0, s72
	s_add_i32 s73, s43, 0x6000
	global_load_lds_dwordx4 v204, s[0:1]
	s_mov_b32 m0, s73
	v_mov_b32_e32 v66, 0
	global_load_lds_dwordx4 v200, s[0:1]
	v_mov_b32_e32 v203, v66
	v_mov_b32_e32 v199, v66
	v_mov_b32_e32 v205, v66
	v_mov_b32_e32 v201, v66
	s_cmp_eq_u32 s3, 1
	s_mov_b32 s74, 0x10000
	v_lshl_add_u64 v[8:9], s[52:53], 0, v[202:203]
	v_lshl_add_u64 v[6:7], s[52:53], 0, v[198:199]
	s_mov_b64 s[0:1], 0x10000
	v_lshl_add_u64 v[2:3], s[46:47], 0, v[204:205]
	s_cselect_b64 s[6:7], -1, 0
	s_cmp_lg_u32 s3, 1
	v_lshl_add_u64 v[4:5], s[46:47], 0, v[200:201]
	s_cbranch_scc1 .LBB0_1755
	s_barrier

;     DI bool next(int i, pg8::GU& u) const { int pm, pn; if (!T.tile(i, pm, pn)) return false; u.pm = pm; u.pn = pn; u.e = 0; u.aux = 0; u.h1 = 0; u.a = A + (size_t)pm * 256 * lda; u.b = Bt + (size_t)pn * 256 * ldb; return true; }
;     DI bool next(int i, pg8::GU& u) const {
;         const int L = i * G + c, T = MT[64 + 32]; if (L >= T * 8) return false;
;         const int rt = L >> 3, ct = L & 7; const int e = MT[192 + rt];
;         const int lt = rt - MT[64 + e];
;         u.e = e; u.pm = lt; u.pn = ct; u.aux = MT[e] + 256 * lt; u.h1 = (MT[128 + e] - 256 * lt) <= 128; u.a = ACT + (size_t)u.aux * lda; u.b = ED + (size_t)e * estride + (size_t)ct * 256 * ldb; return true;
.LBB0_1758:
	ds_read_b32 v3, v213
	s_add_i32 s82, s82, 1
	s_mul_i32 s2, s82, s23
	s_add_i32 s2, s2, s98
	s_waitcnt lgkmcnt(0)
	v_readfirstlane_b32 s3, v3
	s_lshl_b32 s3, s3, 3
	s_cmp_lt_i32 s2, s3
	s_cselect_b64 s[44:45], -1, 0
	s_cmp_ge_i32 s2, s3
	s_cbranch_scc1 .LBB0_1760
	s_ashr_i32 s4, s2, 3
	s_lshl_b32 s3, s4, 2
	s_add_i32 s3, s66, s3
	v_mov_b32_e32 v3, s3
	ds_read_b32 v3, v3 offset:768
	s_and_b32 s88, s2, 7
	s_waitcnt lgkmcnt(0)
	v_lshlrev_b32_e32 v4, 2, v3
	v_add_u32_e32 v6, s66, v4
	ds_read2st64_b32 v[4:5], v6 offset1:1
	v_readfirstlane_b32 s2, v3
	ds_read_b32 v3, v6 offset:512
	s_ashr_i32 s3, s2, 31
	s_waitcnt lgkmcnt(0)
	v_readfirstlane_b32 s5, v5
	s_sub_i32 s4, s4, s5
	v_readfirstlane_b32 s36, v4
	s_lshl_b32 s4, s4, 8
	s_add_i32 s36, s4, s36
	s_ashr_i32 s37, s36, 31
	v_subrev_u32_e32 v3, s4, v3
	s_lshl_b64 s[4:5], s[36:37], 9
	s_add_u32 s38, s60, s4
	s_addc_u32 s39, s61, s5
	s_lshl_b64 s[2:3], s[2:3], 20
	s_add_u32 s2, s62, s2
	s_addc_u32 s3, s63, s3
	s_lshl_b32 s4, s88, 17
	v_cmp_gt_i32_e32 vcc, s81, v3
	s_add_u32 s40, s2, s4
	s_addc_u32 s41, s3, 0
	v_cndmask_b32_e64 v220, 0, 1, vcc
